# prio_late
# speedup vs baseline: 1.0066x; 1.0066x over previous
.LBB3_36:
	global_load_dwordx4 v[58:61], v[114:115], off
	global_load_dwordx4 v[62:65], v[116:117], off
	global_load_dwordx4 v[66:69], v[118:119], off
	global_load_dwordx4 v[70:73], v[120:121], off
	s_waitcnt lgkmcnt(1)
	v_bfe_u32 v76, v231, 23, 8
	s_cmp_eq_u32 s34, 1
	v_max_u32_e32 v76, 11, v76
	s_cselect_b64 s[24:25], -1, 0
	v_lshlrev_b32_e32 v240, 23, v76
	v_cndmask_b32_e64 v76, 2.0, 1.0, s[24:25]
	s_lshl_b32 s8, s34, 16
	v_mul_f32_e32 v230, v76, v230
	s_and_b32 s67, s8, 0x10000
	v_sub_u32_e32 v164, 0x84000000, v240
	v_pk_fma_f32 v[182:183], v[230:231], v[182:183], v[212:213] op_sel_hi:[0,1,1] neg_lo:[0,0,1] neg_hi:[0,0,1]
	v_pk_fma_f32 v[184:185], v[230:231], v[184:185], v[210:211] op_sel_hi:[0,1,1] neg_lo:[0,0,1] neg_hi:[0,0,1]
	v_pk_fma_f32 v[186:187], v[230:231], v[186:187], v[208:209] op_sel_hi:[0,1,1] neg_lo:[0,0,1] neg_hi:[0,0,1]
	v_pk_fma_f32 v[188:189], v[230:231], v[188:189], v[206:207] op_sel_hi:[0,1,1] neg_lo:[0,0,1] neg_hi:[0,0,1]
	v_fma_mixlo_f16 v78, v182, v164, 0 op_sel_hi:[0,0,0]
	v_fma_mixlo_f16 v79, v184, v164, 0 op_sel_hi:[0,0,0]
	v_fma_mixlo_f16 v80, v186, v164, 0 op_sel_hi:[0,0,0]
	v_fma_mixlo_f16 v81, v188, v164, 0 op_sel_hi:[0,0,0]
	v_lshl_add_u32 v82, v246, 4, s67
	v_fma_mixhi_f16 v78, v183, v164, 0 op_sel_hi:[0,0,0]
	v_fma_mixhi_f16 v79, v185, v164, 0 op_sel_hi:[0,0,0]
	v_fma_mixhi_f16 v80, v187, v164, 0 op_sel_hi:[0,0,0]
	v_fma_mixhi_f16 v81, v189, v164, 0 op_sel_hi:[0,0,0]
	ds_write_b128 v82, v[78:81]
	v_pk_fma_f32 v[198:199], v[230:231], v[198:199], v[196:197] op_sel_hi:[0,1,1] neg_lo:[0,0,1] neg_hi:[0,0,1]
	v_pk_fma_f32 v[200:201], v[230:231], v[200:201], v[194:195] op_sel_hi:[0,1,1] neg_lo:[0,0,1] neg_hi:[0,0,1]
	v_pk_fma_f32 v[202:203], v[230:231], v[202:203], v[192:193] op_sel_hi:[0,1,1] neg_lo:[0,0,1] neg_hi:[0,0,1]
	v_pk_fma_f32 v[204:205], v[230:231], v[204:205], v[190:191] op_sel_hi:[0,1,1] neg_lo:[0,0,1] neg_hi:[0,0,1]
	v_fma_mixlo_f16 v78, v198, v164, 0 op_sel_hi:[0,0,0]
	v_fma_mixlo_f16 v79, v200, v164, 0 op_sel_hi:[0,0,0]
	v_fma_mixlo_f16 v80, v202, v164, 0 op_sel_hi:[0,0,0]
	v_fma_mixlo_f16 v81, v204, v164, 0 op_sel_hi:[0,0,0]
	v_lshl_add_u32 v82, v247, 4, s67
	v_fma_mixhi_f16 v78, v199, v164, 0 op_sel_hi:[0,0,0]
	v_fma_mixhi_f16 v79, v201, v164, 0 op_sel_hi:[0,0,0]
	v_fma_mixhi_f16 v80, v203, v164, 0 op_sel_hi:[0,0,0]
	v_fma_mixhi_f16 v81, v205, v164, 0 op_sel_hi:[0,0,0]
	ds_write_b128 v82, v[78:81]
	v_pk_fma_f32 v[214:215], v[230:231], v[214:215], v[180:181] op_sel_hi:[0,1,1] neg_lo:[0,0,1] neg_hi:[0,0,1]
	v_pk_fma_f32 v[216:217], v[230:231], v[216:217], v[178:179] op_sel_hi:[0,1,1] neg_lo:[0,0,1] neg_hi:[0,0,1]
	v_pk_fma_f32 v[218:219], v[230:231], v[218:219], v[176:177] op_sel_hi:[0,1,1] neg_lo:[0,0,1] neg_hi:[0,0,1]
	v_pk_fma_f32 v[220:221], v[230:231], v[220:221], v[174:175] op_sel_hi:[0,1,1] neg_lo:[0,0,1] neg_hi:[0,0,1]
	v_fma_mixlo_f16 v78, v214, v164, 0 op_sel_hi:[0,0,0]
	v_fma_mixlo_f16 v79, v216, v164, 0 op_sel_hi:[0,0,0]
	v_fma_mixlo_f16 v80, v218, v164, 0 op_sel_hi:[0,0,0]
	v_fma_mixlo_f16 v81, v220, v164, 0 op_sel_hi:[0,0,0]
	v_lshl_add_u32 v82, v248, 4, s67
	v_fma_mixhi_f16 v78, v215, v164, 0 op_sel_hi:[0,0,0]
	v_fma_mixhi_f16 v79, v217, v164, 0 op_sel_hi:[0,0,0]
	v_fma_mixhi_f16 v80, v219, v164, 0 op_sel_hi:[0,0,0]
	v_fma_mixhi_f16 v81, v221, v164, 0 op_sel_hi:[0,0,0]
	ds_write_b128 v82, v[78:81]
	v_pk_fma_f32 v[222:223], v[230:231], v[222:223], v[172:173] op_sel_hi:[0,1,1] neg_lo:[0,0,1] neg_hi:[0,0,1]
	v_pk_fma_f32 v[224:225], v[230:231], v[224:225], v[170:171] op_sel_hi:[0,1,1] neg_lo:[0,0,1] neg_hi:[0,0,1]
	v_pk_fma_f32 v[226:227], v[230:231], v[226:227], v[168:169] op_sel_hi:[0,1,1] neg_lo:[0,0,1] neg_hi:[0,0,1]
	v_pk_fma_f32 v[228:229], v[230:231], v[228:229], v[166:167] op_sel_hi:[0,1,1] neg_lo:[0,0,1] neg_hi:[0,0,1]
	v_fma_mixlo_f16 v78, v222, v164, 0 op_sel_hi:[0,0,0]
	v_fma_mixlo_f16 v79, v224, v164, 0 op_sel_hi:[0,0,0]
	v_fma_mixlo_f16 v80, v226, v164, 0 op_sel_hi:[0,0,0]
	v_fma_mixlo_f16 v81, v228, v164, 0 op_sel_hi:[0,0,0]
	v_lshl_add_u32 v82, v249, 4, s67
	v_fma_mixhi_f16 v78, v223, v164, 0 op_sel_hi:[0,0,0]
	v_fma_mixhi_f16 v79, v225, v164, 0 op_sel_hi:[0,0,0]
	v_fma_mixhi_f16 v80, v227, v164, 0 op_sel_hi:[0,0,0]
	v_fma_mixhi_f16 v81, v229, v164, 0 op_sel_hi:[0,0,0]
	v_pk_mul_f32 v[206:207], v[38:39], v[74:75]
	v_pk_mul_f32 v[208:209], v[40:41], v[74:75]
	v_pk_mul_f32 v[210:211], v[34:35], v[74:75]
	v_pk_mul_f32 v[212:213], v[36:37], v[74:75]
	v_pk_mul_f32 v[190:191], v[46:47], v[74:75]
	v_pk_mul_f32 v[192:193], v[48:49], v[74:75]
	v_pk_mul_f32 v[194:195], v[42:43], v[74:75]
	v_pk_mul_f32 v[196:197], v[44:45], v[74:75]
	v_pk_mul_f32 v[174:175], v[54:55], v[74:75]
	v_pk_mul_f32 v[176:177], v[56:57], v[74:75]
	v_pk_mul_f32 v[178:179], v[50:51], v[74:75]
	v_pk_mul_f32 v[180:181], v[52:53], v[74:75]
	v_pk_mul_f32 v[166:167], v[124:125], v[74:75]
	v_pk_mul_f32 v[168:169], v[128:129], v[74:75]
	v_pk_mul_f32 v[170:171], v[126:127], v[74:75]
	v_pk_mul_f32 v[172:173], v[130:131], v[74:75]
	s_setprio 0
	s_andn2_b64 vcc, exec, s[12:13]
	s_mov_b64 s[24:25], -1
	ds_write_b128 v82, v[78:81]
	s_cbranch_vccnz .LBB3_38
	s_mov_b64 s[24:25], 0
